# speedup vs baseline: 1.0069x; 1.0041x over previous
_Z5k_csrPKjS0_PKfPjPfPDF16_P15HIP_vector_typeIjLj4EE:
	s_load_dwordx2 s[4:5], s[0:1], 0x0
	s_load_dwordx2 s[6:7], s[0:1], 0x10
	s_mul_i32 s3, s2, 0xc4
	v_lshrrev_b32_e32 v25, 4, v0
	v_add_u32_e32 v28, s3, v25
	v_and_b32_e32 v1, 15, v0
	v_min_i32_e32 v4, 0xc34f, v28
	v_add_u32_e32 v26, 64, v28
	v_lshlrev_b32_e32 v18, 4, v1
	v_mov_b32_e32 v19, 0
	v_ashrrev_i32_e32 v5, 31, v4
	v_min_i32_e32 v6, 0xc34f, v26
	s_waitcnt lgkmcnt(0)
	v_lshrrev_b32_e32 v56, 3, v0
	v_min_u32_e32 v56, 0x7c, v56
	s_mul_i32 s40, s2, 0x7d
	v_add_u32_e32 v56, s40, v56
	v_mov_b32_e32 v57, 0
	v_lshl_add_u64 v[56:57], v[56:57], 2, s[4:5]
	global_load_dword v58, v[56:57], off
	global_load_dword v59, v[56:57], off offset:500
	v_lshl_add_u64 v[2:3], s[6:7], 0, v[18:19]
	v_lshlrev_b64 v[4:5], 8, v[4:5]
	v_ashrrev_i32_e32 v7, 31, v6
	v_lshl_add_u64 v[4:5], v[2:3], 0, v[4:5]
	v_lshlrev_b64 v[6:7], 8, v[6:7]
	v_add_u32_e32 v24, 0x80, v28
	v_lshl_add_u64 v[6:7], v[2:3], 0, v[6:7]
	global_load_dwordx4 v[14:17], v[4:5], off nt
	global_load_dwordx4 v[10:13], v[6:7], off nt
	v_min_i32_e32 v4, 0xc34f, v24
	v_or_b32_e32 v32, 0xc00, v0
	v_ashrrev_i32_e32 v5, 31, v4
	v_lshrrev_b32_e32 v23, 4, v32
	v_lshlrev_b64 v[4:5], 8, v[4:5]
	v_add_u32_e32 v22, s3, v23
	v_lshl_add_u64 v[20:21], v[2:3], 0, v[4:5]
	v_min_i32_e32 v4, 0xc34f, v22
	v_ashrrev_i32_e32 v5, 31, v4
	v_lshlrev_b64 v[4:5], 8, v[4:5]
	v_lshrrev_b32_e32 v1, 3, v0
	v_lshl_add_u64 v[30:31], v[2:3], 0, v[4:5]
	global_load_dwordx4 v[6:9], v[20:21], off nt
	global_load_dwordx4 v[2:5], v[30:31], off nt
	v_min_u32_e32 v20, 0x7c, v1
	s_mul_i32 s6, s2, 0x7d
	v_add_u32_e32 v30, s6, v20
	v_ashrrev_i32_e32 v31, 31, v30
	v_lshl_add_u64 v[30:31], v[30:31], 2, s[4:5]
	v_cmp_gt_u32_e32 vcc, 2, v0
	v_lshlrev_b32_e32 v1, 2, v0
	s_and_saveexec_b64 s[4:5], vcc
	v_lshlrev_b32_e32 v18, 2, v0
	ds_write_b32 v18, v19 offset:22528
	s_or_b64 exec, exec, s[4:5]
	s_movk_i32 s4, 0x100
	v_cmp_gt_u32_e64 s[8:9], s4, v0
	s_and_saveexec_b64 s[4:5], s[8:9]
	s_cbranch_execz .LBB1_4
	s_mov_b32 s6, 0x539782a
	v_mul_hi_u32 v29, v0, s6
	s_movk_i32 s6, 0xffcf
	v_lshlrev_b32_e32 v18, 2, v0
	v_mov_b32_e32 v19, 0
	v_mad_i32_i24 v29, v29, s6, v0
	ds_write2st64_b32 v18, v19, v29 offset0:64 offset1:72
.LBB1_4:
	s_or_b64 exec, exec, s[4:5]
	s_load_dwordx2 s[26:27], s[0:1], 0x8
	s_load_dwordx4 s[28:31], s[0:1], 0x18
	s_load_dwordx2 s[36:37], s[0:1], 0x30
	v_and_b32_e32 v18, 7, v0
	s_movk_i32 s4, 0x3e8
	v_cmp_gt_u32_e32 vcc, s4, v0
	v_cmp_eq_u32_e64 s[4:5], 0, v18
	s_waitcnt vmcnt(4)
	v_mov_b32_e32 v21, v58
	v_mov_b32_e32 v27, v59
	v_sub_u32_e32 v19, v27, v21
	s_mov_b32 s11, 0
	s_and_b64 s[4:5], s[4:5], vcc
	s_waitcnt lgkmcnt(0)
	s_barrier
	s_and_saveexec_b64 s[6:7], s[4:5]
	s_cbranch_execz .LBB1_13
	s_mov_b64 s[4:5], exec

amdhsa.kernels:
  - .agpr_count:     0
    .args:
      - .actual_access:  read_only
        .address_space:  global
        .offset:         0
        .size:           8
        .value_kind:     global_buffer
      - .actual_access:  read_only
        .address_space:  global
        .offset:         8
        .size:           8
        .value_kind:     global_buffer
      - .actual_access:  write_only
        .address_space:  global
        .offset:         16
        .size:           8
        .value_kind:     global_buffer
      - .actual_access:  write_only
        .address_space:  global
        .offset:         24
        .size:           8
        .value_kind:     global_buffer
      - .actual_access:  read_only
        .address_space:  global
        .offset:         32
        .size:           8
        .value_kind:     global_buffer
      - .actual_access:  read_only
        .address_space:  global
        .offset:         40
        .size:           8
        .value_kind:     global_buffer
      - .actual_access:  read_only
        .address_space:  global
        .offset:         48
        .size:           8
        .value_kind:     global_buffer
      - .actual_access:  read_only
        .address_space:  global
        .offset:         56
        .size:           8
        .value_kind:     global_buffer
      - .actual_access:  read_only
        .address_space:  global
        .offset:         64
        .size:           8
        .value_kind:     global_buffer
      - .actual_access:  write_only
        .address_space:  global
        .offset:         72
        .size:           8
        .value_kind:     global_buffer
      - .actual_access:  write_only
        .address_space:  global
        .offset:         80
        .size:           8
        .value_kind:     global_buffer
      - .actual_access:  write_only
        .address_space:  global
        .offset:         88
        .size:           8
        .value_kind:     global_buffer
      - .actual_access:  write_only
        .address_space:  global
        .offset:         96
        .size:           8
        .value_kind:     global_buffer
      - .actual_access:  write_only
        .address_space:  global
        .offset:         104
        .size:           8
        .value_kind:     global_buffer
      - .actual_access:  write_only
        .address_space:  global
        .offset:         112
        .size:           8
        .value_kind:     global_buffer
      - .offset:         120
        .size:           4
        .value_kind:     hidden_block_count_x
      - .offset:         124
        .size:           4
        .value_kind:     hidden_block_count_y
      - .offset:         128
        .size:           4
        .value_kind:     hidden_block_count_z
      - .offset:         132
        .size:           2
        .value_kind:     hidden_group_size_x
      - .offset:         134
        .size:           2
        .value_kind:     hidden_group_size_y
      - .offset:         136
        .size:           2
        .value_kind:     hidden_group_size_z
      - .offset:         138
        .size:           2
        .value_kind:     hidden_remainder_x
      - .offset:         140
        .size:           2
        .value_kind:     hidden_remainder_y
      - .offset:         142
        .size:           2
        .value_kind:     hidden_remainder_z
      - .offset:         160
        .size:           8
        .value_kind:     hidden_global_offset_x
      - .offset:         168
        .size:           8
        .value_kind:     hidden_global_offset_y
      - .offset:         176
        .size:           8
        .value_kind:     hidden_global_offset_z
      - .offset:         184
        .size:           2
        .value_kind:     hidden_grid_dims
    .group_segment_fixed_size: 21520
    .kernarg_segment_align: 8
    .kernarg_segment_size: 376
    .language:       OpenCL C
    .language_version:
      - 2
      - 0
    .max_flat_workgroup_size: 1024
    .name:           _Z11k_chunksortPKiS0_PjS1_PKfS3_S3_S3_S3_PDF16_S4_PfS5_S4_Ph
    .private_segment_fixed_size: 0
    .sgpr_count:     32
    .sgpr_spill_count: 0
    .symbol:         _Z11k_chunksortPKiS0_PjS1_PKfS3_S3_S3_S3_PDF16_S4_PfS5_S4_Ph.kd
    .uniform_work_group_size: 1
    .uses_dynamic_stack: false
    .vgpr_count:     38
    .vgpr_spill_count: 0
    .wavefront_size: 64
  - .agpr_count:     0
    .args:
      - .actual_access:  read_only
        .address_space:  global
        .offset:         0
        .size:           8
        .value_kind:     global_buffer
      - .actual_access:  read_only
        .address_space:  global
        .offset:         8
        .size:           8
        .value_kind:     global_buffer
      - .actual_access:  read_only
        .address_space:  global
        .offset:         16
        .size:           8
        .value_kind:     global_buffer
      - .actual_access:  write_only
        .address_space:  global
        .offset:         24
        .size:           8
        .value_kind:     global_buffer
      - .actual_access:  write_only
        .address_space:  global
        .offset:         32
        .size:           8
        .value_kind:     global_buffer
      - .actual_access:  write_only
        .address_space:  global
        .offset:         40
        .size:           8
        .value_kind:     global_buffer
      - .actual_access:  write_only
        .address_space:  global
        .offset:         48
        .size:           8
        .value_kind:     global_buffer
    .group_segment_fixed_size: 22536
    .kernarg_segment_align: 8
    .kernarg_segment_size: 56
    .language:       OpenCL C
    .language_version:
      - 2
      - 0
    .max_flat_workgroup_size: 1024
    .name:           _Z5k_csrPKjS0_PKfPjPfPDF16_P15HIP_vector_typeIjLj4EE
    .private_segment_fixed_size: 0
    .sgpr_count:     54
    .sgpr_spill_count: 0
    .symbol:         _Z5k_csrPKjS0_PKfPjPfPDF16_P15HIP_vector_typeIjLj4EE.kd
    .uniform_work_group_size: 1
    .uses_dynamic_stack: false
    .vgpr_count:     64
    .vgpr_spill_count: 0
    .wavefront_size: 64
  - .agpr_count:     0
    .args:
      - .actual_access:  read_only
        .address_space:  global
        .offset:         0
        .size:           8
        .value_kind:     global_buffer
      - .actual_access:  read_only
        .address_space:  global
        .offset:         8
        .size:           8
        .value_kind:     global_buffer
      - .actual_access:  read_only
        .address_space:  global
        .offset:         16
        .size:           8
        .value_kind:     global_buffer
      - .actual_access:  read_only
        .address_space:  global
        .offset:         24
        .size:           8
        .value_kind:     global_buffer
      - .actual_access:  read_only
        .address_space:  global
        .offset:         32
        .size:           8
        .value_kind:     global_buffer
      - .actual_access:  read_only
        .address_space:  global
        .offset:         40
        .size:           8
        .value_kind:     global_buffer
      - .actual_access:  read_only
        .address_space:  global
        .offset:         48
        .size:           8
        .value_kind:     global_buffer
      - .actual_access:  write_only
        .address_space:  global
        .offset:         56
        .size:           8
        .value_kind:     global_buffer
      - .actual_access:  write_only
        .address_space:  global
        .offset:         64
        .size:           8
        .value_kind:     global_buffer
    .group_segment_fixed_size: 36112
    .kernarg_segment_align: 8
    .kernarg_segment_size: 72
    .language:       OpenCL C
    .language_version:
      - 2
      - 0
    .max_flat_workgroup_size: 256
    .name:           _Z8k_layer1PKfPKDF16_PK15HIP_vector_typeIjLj4EEPKjS0_S2_S0_PhPf
    .private_segment_fixed_size: 0
    .sgpr_count:     30
    .sgpr_spill_count: 0
    .symbol:         _Z8k_layer1PKfPKDF16_PK15HIP_vector_typeIjLj4EEPKjS0_S2_S0_PhPf.kd
    .uniform_work_group_size: 1
    .uses_dynamic_stack: false
    .vgpr_count:     128
    .vgpr_spill_count: 0
    .wavefront_size: 64
  - .agpr_count:     0
    .args:
      - .actual_access:  read_only
        .address_space:  global
        .offset:         0
        .size:           8
        .value_kind:     global_buffer
      - .actual_access:  read_only
        .address_space:  global
        .offset:         8
        .size:           8
        .value_kind:     global_buffer
      - .actual_access:  read_only
        .address_space:  global
        .offset:         16
        .size:           8
        .value_kind:     global_buffer
      - .actual_access:  read_only
        .address_space:  global
        .offset:         24
        .size:           8
        .value_kind:     global_buffer
      - .actual_access:  read_only
        .address_space:  global
        .offset:         32
        .size:           8
        .value_kind:     global_buffer
      - .actual_access:  read_only
        .address_space:  global
        .offset:         40
        .size:           8
        .value_kind:     global_buffer
      - .actual_access:  read_only
        .address_space:  global
        .offset:         48
        .size:           8
        .value_kind:     global_buffer
      - .address_space:  global
        .offset:         56
        .size:           8
        .value_kind:     global_buffer
    .group_segment_fixed_size: 39168
    .kernarg_segment_align: 8
    .kernarg_segment_size: 64
    .language:       OpenCL C
    .language_version:
      - 2
      - 0
    .max_flat_workgroup_size: 256
    .name:           _Z8k_layer2PKhPKfPK15HIP_vector_typeIjLj4EEPKjS2_PKDF16_S2_Pf
    .private_segment_fixed_size: 0
    .sgpr_count:     27
    .sgpr_spill_count: 0
    .symbol:         _Z8k_layer2PKhPKfPK15HIP_vector_typeIjLj4EEPKjS2_PKDF16_S2_Pf.kd
    .uniform_work_group_size: 1
    .uses_dynamic_stack: false
    .vgpr_count:     112
    .vgpr_spill_count: 0
    .wavefront_size: 64
  - .agpr_count:     0
    .args:
      - .actual_access:  read_only
        .address_space:  global
        .offset:         0
        .size:           8
        .value_kind:     global_buffer
      - .actual_access:  read_only
        .address_space:  global
        .offset:         8
        .size:           8
        .value_kind:     global_buffer
      - .actual_access:  read_only
        .address_space:  global
        .offset:         16
        .size:           8
        .value_kind:     global_buffer
      - .actual_access:  read_only
        .address_space:  global
        .offset:         24
        .size:           8
        .value_kind:     global_buffer
      - .actual_access:  read_only
        .address_space:  global
        .offset:         32
        .size:           8
        .value_kind:     global_buffer
      - .actual_access:  write_only
        .address_space:  global
        .offset:         40
        .size:           8
        .value_kind:     global_buffer
    .group_segment_fixed_size: 512
    .kernarg_segment_align: 8
    .kernarg_segment_size: 48
    .language:       OpenCL C
    .language_version:
      - 2
      - 0
    .max_flat_workgroup_size: 320
    .name:           _Z7k_headsPKfS0_S0_S0_S0_Pf
    .private_segment_fixed_size: 0
    .sgpr_count:     22
    .sgpr_spill_count: 0
    .symbol:         _Z7k_headsPKfS0_S0_S0_S0_Pf.kd
    .uniform_work_group_size: 1
    .uses_dynamic_stack: false
    .vgpr_count:     56
    .vgpr_spill_count: 0
    .wavefront_size: 64
